# v135 plus MoE weight-conversion loop: 32 serialized LDS transposing reads per item batched into 4 groups of 8 distinct VGPR pairs
# baseline (speedup 1.0000x reference)
.LBB0_321:
	ds_read2_b32 v[108:109], v71 offset1:68
	ds_read2_b32 v[110:111], v71 offset0:136 offset1:204
	v_add_u32_e32 v140, 0x400, v71
	v_add_u32_e32 v141, 0x800, v71
	v_add_u32_e32 v142, 0xc00, v71
	ds_read2_b32 v[112:113], v140 offset0:16 offset1:84
	ds_read2_b32 v[114:115], v140 offset0:152 offset1:220
	ds_read2_b32 v[116:117], v141 offset0:32 offset1:100
	ds_read2_b32 v[118:119], v141 offset0:168 offset1:236
	ds_read2_b32 v[120:121], v142 offset0:48 offset1:116
	ds_read2_b32 v[122:123], v142 offset0:184 offset1:252
	s_lshl_b32 s5, s10, 1
	s_and_b32 s5, s5, 0xffffff00
	s_and_b32 s12, s10, 0x7f
	s_cmp_eq_u32 s28, 2
	s_cselect_b32 s13, 0x80, 0
	s_or_b32 s5, s5, s12
	s_or_b32 s5, s5, s13
	s_cmp_eq_u32 s28, 0
	s_cselect_b32 s5, s10, s5
	s_ashr_i32 s10, s29, 31
	s_add_u32 s8, s8, s29
	s_addc_u32 s9, s9, s10
	v_lshl_add_u64 v[100:101], s[8:9], 0, v[64:65]
	s_and_b64 vcc, exec, s[6:7]
	s_mov_b32 s10, s4
	s_mov_b32 s28, s22
	s_mov_b32 s29, s25
	s_waitcnt lgkmcnt(0)
	v_mul_f32_e32 v108, 0x42800000, v108
	v_mul_f32_e32 v109, 0x42800000, v109
	v_mul_f32_e32 v110, 0x42800000, v110
	v_mul_f32_e32 v111, 0x42800000, v111
	v_mul_f32_e32 v112, 0x42800000, v112
	v_mul_f32_e32 v113, 0x42800000, v113
	v_mul_f32_e32 v114, 0x42800000, v114
	v_mul_f32_e32 v115, 0x42800000, v115
	v_mul_f32_e32 v116, 0x42800000, v116
	v_mul_f32_e32 v117, 0x42800000, v117
	v_mul_f32_e32 v118, 0x42800000, v118
	v_mul_f32_e32 v119, 0x42800000, v119
	v_mul_f32_e32 v120, 0x42800000, v120
	v_mul_f32_e32 v121, 0x42800000, v121
	v_mul_f32_e32 v122, 0x42800000, v122
	v_mul_f32_e32 v123, 0x42800000, v123
	v_mov_b32_e32 v102, v97
	v_mov_b32_e32 v103, v97
	v_mov_b32_e32 v104, v97
	v_mov_b32_e32 v105, v97
	v_cvt_pk_fp8_f32 v102, v108, v109
	v_cvt_pk_fp8_f32 v103, v112, v113
	v_cvt_pk_fp8_f32 v104, v116, v117
	v_cvt_pk_fp8_f32 v105, v120, v121
	v_cvt_pk_fp8_f32 v102, v110, v111 op_sel:[0,0,1]
	v_cvt_pk_fp8_f32 v103, v114, v115 op_sel:[0,0,1]
	v_cvt_pk_fp8_f32 v104, v118, v119 op_sel:[0,0,1]
	v_cvt_pk_fp8_f32 v105, v122, v123 op_sel:[0,0,1]
	s_nop 0
	v_add_u32_e32 v93, s5, v69
	v_mad_i64_i32 v[106:107], s[8:9], v93, s41, v[100:101]
	global_store_dwordx4 v[106:107], v[102:105], off
	ds_read2_b32 v[108:109], v83 offset1:68
	ds_read2_b32 v[110:111], v83 offset0:136 offset1:204
	v_add_u32_e32 v140, 0x400, v83
	v_add_u32_e32 v141, 0x800, v83
	v_add_u32_e32 v142, 0xc00, v83
	ds_read2_b32 v[112:113], v140 offset0:16 offset1:84
	ds_read2_b32 v[114:115], v140 offset0:152 offset1:220
	ds_read2_b32 v[116:117], v141 offset0:32 offset1:100
	ds_read2_b32 v[118:119], v141 offset0:168 offset1:236
	ds_read2_b32 v[120:121], v142 offset0:48 offset1:116
	ds_read2_b32 v[122:123], v142 offset0:184 offset1:252
	s_waitcnt lgkmcnt(0)
	v_mul_f32_e32 v108, 0x42800000, v108
	v_mul_f32_e32 v109, 0x42800000, v109
	v_mul_f32_e32 v110, 0x42800000, v110
	v_mul_f32_e32 v111, 0x42800000, v111
	v_mul_f32_e32 v112, 0x42800000, v112
	v_mul_f32_e32 v113, 0x42800000, v113
	v_mul_f32_e32 v114, 0x42800000, v114
	v_mul_f32_e32 v115, 0x42800000, v115
	v_mul_f32_e32 v116, 0x42800000, v116
	v_mul_f32_e32 v117, 0x42800000, v117
	v_mul_f32_e32 v118, 0x42800000, v118
	v_mul_f32_e32 v119, 0x42800000, v119
	v_mul_f32_e32 v120, 0x42800000, v120
	v_mul_f32_e32 v121, 0x42800000, v121
	v_mul_f32_e32 v122, 0x42800000, v122
	v_mul_f32_e32 v123, 0x42800000, v123
	v_mov_b32_e32 v102, v97
	v_mov_b32_e32 v103, v97
	v_mov_b32_e32 v104, v97
	v_mov_b32_e32 v105, v97
	v_cvt_pk_fp8_f32 v102, v108, v109
	v_cvt_pk_fp8_f32 v103, v112, v113
	v_cvt_pk_fp8_f32 v104, v116, v117
	v_cvt_pk_fp8_f32 v105, v120, v121
	v_cvt_pk_fp8_f32 v102, v110, v111 op_sel:[0,0,1]
	v_cvt_pk_fp8_f32 v103, v114, v115 op_sel:[0,0,1]
	v_cvt_pk_fp8_f32 v104, v118, v119 op_sel:[0,0,1]
	v_cvt_pk_fp8_f32 v105, v122, v123 op_sel:[0,0,1]
	s_nop 0
	v_add_u32_e32 v93, s5, v81
	v_mad_i64_i32 v[106:107], s[8:9], v93, s41, v[100:101]
	global_store_dwordx4 v[106:107], v[102:105], off
	ds_read2_b32 v[108:109], v87 offset1:68
	ds_read2_b32 v[110:111], v87 offset0:136 offset1:204
	v_add_u32_e32 v140, 0x400, v87
	v_add_u32_e32 v141, 0x800, v87
	v_add_u32_e32 v142, 0xc00, v87
	ds_read2_b32 v[112:113], v140 offset0:16 offset1:84
	ds_read2_b32 v[114:115], v140 offset0:152 offset1:220
	ds_read2_b32 v[116:117], v141 offset0:32 offset1:100
	ds_read2_b32 v[118:119], v141 offset0:168 offset1:236
	ds_read2_b32 v[120:121], v142 offset0:48 offset1:116
	ds_read2_b32 v[122:123], v142 offset0:184 offset1:252
	s_waitcnt lgkmcnt(0)
	v_mul_f32_e32 v108, 0x42800000, v108
	v_mul_f32_e32 v109, 0x42800000, v109
	v_mul_f32_e32 v110, 0x42800000, v110
	v_mul_f32_e32 v111, 0x42800000, v111
	v_mul_f32_e32 v112, 0x42800000, v112
	v_mul_f32_e32 v113, 0x42800000, v113
	v_mul_f32_e32 v114, 0x42800000, v114
	v_mul_f32_e32 v115, 0x42800000, v115
	v_mul_f32_e32 v116, 0x42800000, v116
	v_mul_f32_e32 v117, 0x42800000, v117
	v_mul_f32_e32 v118, 0x42800000, v118
	v_mul_f32_e32 v119, 0x42800000, v119
	v_mul_f32_e32 v120, 0x42800000, v120
	v_mul_f32_e32 v121, 0x42800000, v121
	v_mul_f32_e32 v122, 0x42800000, v122
	v_mul_f32_e32 v123, 0x42800000, v123
	v_mov_b32_e32 v102, v97
	v_mov_b32_e32 v103, v97
	v_mov_b32_e32 v104, v97
	v_mov_b32_e32 v105, v97
	v_cvt_pk_fp8_f32 v102, v108, v109
	v_cvt_pk_fp8_f32 v103, v112, v113
	v_cvt_pk_fp8_f32 v104, v116, v117
	v_cvt_pk_fp8_f32 v105, v120, v121
	v_cvt_pk_fp8_f32 v102, v110, v111 op_sel:[0,0,1]
	v_cvt_pk_fp8_f32 v103, v114, v115 op_sel:[0,0,1]
	v_cvt_pk_fp8_f32 v104, v118, v119 op_sel:[0,0,1]
	v_cvt_pk_fp8_f32 v105, v122, v123 op_sel:[0,0,1]
	s_nop 0
	v_add_u32_e32 v93, s5, v85
	v_mad_i64_i32 v[106:107], s[8:9], v93, s41, v[100:101]
	global_store_dwordx4 v[106:107], v[102:105], off
	ds_read2_b32 v[108:109], v91 offset1:68
	ds_read2_b32 v[110:111], v91 offset0:136 offset1:204
	v_add_u32_e32 v140, 0x400, v91
	v_add_u32_e32 v141, 0x800, v91
	v_add_u32_e32 v142, 0xc00, v91
	ds_read2_b32 v[112:113], v140 offset0:16 offset1:84
	ds_read2_b32 v[114:115], v140 offset0:152 offset1:220
	ds_read2_b32 v[116:117], v141 offset0:32 offset1:100
	ds_read2_b32 v[118:119], v141 offset0:168 offset1:236
	ds_read2_b32 v[120:121], v142 offset0:48 offset1:116
	ds_read2_b32 v[122:123], v142 offset0:184 offset1:252
	s_waitcnt lgkmcnt(0)
	v_mul_f32_e32 v108, 0x42800000, v108
	v_mul_f32_e32 v109, 0x42800000, v109
	v_mul_f32_e32 v110, 0x42800000, v110
	v_mul_f32_e32 v111, 0x42800000, v111
	v_mul_f32_e32 v112, 0x42800000, v112
	v_mul_f32_e32 v113, 0x42800000, v113
	v_mul_f32_e32 v114, 0x42800000, v114
	v_mul_f32_e32 v115, 0x42800000, v115
	v_mul_f32_e32 v116, 0x42800000, v116
	v_mul_f32_e32 v117, 0x42800000, v117
	v_mul_f32_e32 v118, 0x42800000, v118
	v_mul_f32_e32 v119, 0x42800000, v119
	v_mul_f32_e32 v120, 0x42800000, v120
	v_mul_f32_e32 v121, 0x42800000, v121
	v_mul_f32_e32 v122, 0x42800000, v122
	v_mul_f32_e32 v123, 0x42800000, v123
	v_mov_b32_e32 v102, v97
	v_mov_b32_e32 v103, v97
	v_mov_b32_e32 v104, v97
	v_mov_b32_e32 v105, v97
	v_cvt_pk_fp8_f32 v102, v108, v109
	v_cvt_pk_fp8_f32 v103, v112, v113
	v_cvt_pk_fp8_f32 v104, v116, v117
	v_cvt_pk_fp8_f32 v105, v120, v121
	v_cvt_pk_fp8_f32 v102, v110, v111 op_sel:[0,0,1]
	v_cvt_pk_fp8_f32 v103, v114, v115 op_sel:[0,0,1]
	v_cvt_pk_fp8_f32 v104, v118, v119 op_sel:[0,0,1]
	v_cvt_pk_fp8_f32 v105, v122, v123 op_sel:[0,0,1]
	s_nop 0
	v_add_u32_e32 v93, s5, v89
	v_mad_i64_i32 v[100:101], s[8:9], v93, s41, v[100:101]
	global_store_dwordx4 v[100:101], v[102:105], off
	s_waitcnt lgkmcnt(0)
	s_mov_b32 s5, s72
	s_mov_b64 s[8:9], s[2:3]
	s_mov_b32 s41, s23
	s_cbranch_vccnz .LBB0_327
